# GLU projection: bid rotated so that an XCD owns 8 consecutive M-tiles with all 4 N-tiles
# speedup vs baseline: 1.0081x; 1.0019x over previous
;     template <int BM> __device__ __forceinline__ void init(const bfr* base, int ld, int row0, int maxrow, const int* ridx) {
; #pragma unroll
;         for (int i = 0; i < (BM * 4 + NTHR - 1) / NTHR; ++i) {
;             const int id = threadIdx.x + i * NTHR, kc = id & 3;
;             int r = id >> 2; if (r > BM - 1) r = BM - 1;
;             int row = ridx ? ridx[r] : row0 + r;
;             if (row > maxrow) row = maxrow;
;             p[i] = base + (size_t)row * ld + kc * 8;
;         }
;     }
;     template <int BN> __device__ __forceinline__ void init(const bfr* base, int ld, int n0) {
; #pragma unroll
;         for (int i = 0; i < BN * 4 / NTHR; ++i) {
;             const int id = threadIdx.x + i * NTHR, r = id >> 2, kc = id & 3;
;             p[i] = base + (size_t)(n0 + r) * ld + kc * 8;
;         }
; __device__ __forceinline__ void phase_glu(const Params& P, bfr* smem, int bid, int nb) {
;     ...
;     int u = bid;
;     if (u < nu) { al.init<256>(Y5, 512, (u >> 2) * 256, LSEQ - 1, nullptr); bl.init<128>(Bt, 512, (u & 3) * 128); gp.prefetch(al, bl); }
.LBB0_2056:
	s_cmp_lt_i32 s6, 15
	s_cselect_b64 s[0:1], -1, 0
	s_cmp_gt_i32 s7, 14
	s_cselect_b64 s[2:3], -1, 0
	s_and_b64 s[0:1], s[0:1], s[2:3]
	s_andn2_b64 vcc, exec, s[0:1]
	s_cbranch_vccnz .LBB0_2118
	v_readlane_b32 s96, v253, 10
	s_cmpk_lg_u32 s96, 0x100
	s_mov_b32 s96, s44
	s_cbranch_scc1 .Lglx
	s_and_b32 s96, s44, 7
	s_lshl_b32 s96, s96, 5
	s_lshr_b32 s97, s44, 3
	s_or_b32 s96, s96, s97
.Lglx:
	s_cmpk_gt_i32 s96, 0xff
	s_cbranch_scc1 .LBB0_2064
	s_add_u32 s0, s42, 0x3b152400
	s_addc_u32 s1, s43, 0
	s_add_u32 s2, s42, 0xda8000
	s_addc_u32 s3, s43, 0
	s_lshl_b32 s6, s96, 6
	s_and_b32 s4, s6, 0xffffff00
	s_waitcnt vmcnt(5)
	v_lshrrev_b32_e32 v116, 2, v0
	v_lshlrev_b32_e32 v1, 3, v0
	v_or_b32_e32 v2, s4, v116
	v_and_b32_e32 v4, 24, v1
	v_min_i32_e32 v2, 0x3fff, v2
	s_waitcnt vmcnt(4)
	v_lshlrev_b32_e32 v102, 1, v4
	v_mov_b32_e32 v103, 0
	s_waitcnt lgkmcnt(1)
	v_ashrrev_i32_e32 v3, 31, v2
	v_lshl_add_u64 v[104:105], s[0:1], 0, v[102:103]
	v_lshlrev_b64 v[2:3], 10, v[2:3]
	v_lshl_add_u64 v[106:107], v[104:105], 0, v[2:3]
	v_or_b32_e32 v2, 0x200, v0
	v_lshrrev_b32_e32 v117, 2, v2
	v_or_b32_e32 v2, s4, v117
	v_min_i32_e32 v2, 0x3fff, v2
	v_ashrrev_i32_e32 v3, 31, v2
	s_lshl_b32 s4, s96, 7
	v_lshlrev_b64 v[2:3], 10, v[2:3]
	s_and_b32 s4, s4, 0x180
	v_lshl_add_u64 v[108:109], v[104:105], 0, v[2:3]
	v_or_b32_e32 v2, s4, v116
	v_lshlrev_b32_e32 v2, 10, v2
	v_mov_b32_e32 v3, v103
	v_lshl_add_u64 v[2:3], s[2:3], 0, v[2:3]
	v_lshl_add_u64 v[110:111], v[2:3], 0, v[102:103]
	global_load_dwordx4 v[90:93], v[108:109], off
	global_load_dwordx4 v[66:69], v[108:109], off offset:64
	global_load_dwordx4 v[94:97], v[110:111], off
	global_load_dwordx4 v[70:73], v[110:111], off offset:64
	global_load_dwordx4 v[74:77], v[106:107], off offset:64
	global_load_dwordx4 v[78:81], v[106:107], off offset:128
	global_load_dwordx4 v[86:89], v[108:109], off offset:128
	global_load_dwordx4 v[98:101], v[106:107], off
	global_load_dwordx4 v[82:85], v[110:111], off offset:128
	v_mad_u32_u24 v3, v117, 40, v4
	v_mul_u32_u24_e32 v2, 40, v116
	v_lshl_add_u32 v119, v3, 1, 0
	v_lshrrev_b32_e32 v3, 1, v0
	v_add_lshl_u32 v2, v2, v4, 1
	v_and_b32_e32 v3, 0xc0, v3
	v_and_b32_e32 v4, 31, v0
	s_waitcnt lgkmcnt(0)
	v_or_b32_e32 v5, v3, v4
	v_and_b32_e32 v6, 8, v116
	v_mul_u32_u24_e32 v5, 40, v5
	v_lshl_add_u32 v7, v6, 1, 0
	v_lshl_add_u32 v121, v5, 1, v7
	v_and_b32_e32 v5, 0x5f, v0
	v_mov_b32_e32 v11, 0x500
	v_mul_u32_u24_e32 v8, 0x50, v5
	v_mul_u32_u24_e32 v9, 40, v5
	v_mad_u32_u24 v5, v5, 40, v11
	v_add_lshl_u32 v10, v9, v6, 1
	v_add_lshl_u32 v11, v5, v6, 1
	v_or_b32_e32 v6, 16, v6
	s_add_i32 s4, 0, 0x11810
	v_add_lshl_u32 v12, v6, v9, 1
	v_add_lshl_u32 v5, v5, v6, 1
	v_add_u32_e32 v120, s4, v2
	v_add_u32_e32 v122, s4, v10
	v_add_u32_e32 v123, s4, v11
	v_add_u32_e32 v124, s4, v12
	v_add_u32_e32 v125, s4, v5
	s_add_i32 s4, 0, 0x14010
	s_waitcnt vmcnt(9)
	v_add_u32_e32 v130, s4, v5
	v_lshrrev_b32_e32 v5, 3, v0
	v_add_u32_e32 v118, 0, v2
	v_add_u32_e32 v126, s4, v2
	v_and_b32_e32 v2, 64, v0
	v_and_or_b32 v3, v5, 4, v3
	v_lshl_add_u32 v2, v2, 2, 0
	v_lshlrev_b32_e32 v4, 2, v4
	v_mul_u32_u24_e32 v3, 0x210, v3
	v_add3_u32 v133, v2, v4, v3
	v_and_b32_e32 v2, 15, v0
	v_lshl_add_u64 v[112:113], s[2:3], 0, v[102:103]
	s_movk_i32 s2, 0x210
	v_lshrrev_b32_e32 v135, 4, v0
	v_lshlrev_b32_e32 v2, 5, v2
	v_mad_u32_u24 v2, v135, s2, v2
	v_readlane_b32 s2, v253, 10
	v_add_u32_e32 v127, s4, v10
	v_add_u32_e32 v128, s4, v11
	v_add_u32_e32 v129, s4, v12
	v_lshl_add_u32 v131, v9, 1, v7
	v_add_u32_e32 v132, 0, v12
	v_or_b32_e32 v134, 0xfffffe00, v0
	v_add3_u32 v136, v2, 0, 16
	s_lshl_b32 s7, s2, 6
	v_add_u32_e32 v137, v7, v8
	s_movk_i32 s8, 0xdff
	s_mov_b32 s4, s96
	v_readlane_b32 s3, v253, 11
